# cache policy: P4 residual loads and the final RMSNorm phase's row loads / f32 output stores made non-temporal
# baseline (speedup 1.0000x reference)
; __device__ __forceinline__ unsigned cvt_pk_bf16(float lo, float hi) { f32x2_t v = {lo, hi}; bf16x2_t b = __builtin_convertvector(v, bf16x2_t); return __builtin_bit_cast(unsigned, b); }
; __device__ __forceinline__ float bf_lo(unsigned w) { return __uint_as_float(w << 16); }
; __device__ __forceinline__ float bf_hi(unsigned w) { return __uint_as_float(w & 0xffff0000u); }
;     __device__ __forceinline__ void operator()(const f32x4 (&acc)[2][2][4][2], const Unit& u, int wr, int wc, int fr, int fq) const {
;     ...
;             for (int i = 0; i < 16; ++i) { const int m = i >> 2, bj = (i >> 1) & 1, n = i & 1; const size_t o = (size_t)(row0 + ai * HALF + m * 16) * cfg::DM + col0 + bj * HALF + n * 16;
;                 if (OLD_BF16) { const u32x2 ww = *(const u32x2*)(xoldb + o); xo[i] = (f32x4){bf_lo(ww.x), bf_hi(ww.x), bf_lo(ww.y), bf_hi(ww.y)}; } else xo[i] = *(const f32x4*)(xold + o); }
;             asm volatile("" ::: "memory");
; #pragma unroll
;             for (int m = 0; m < 4; ++m) { const int r = row0 + ai * HALF + m * 16; float s = 0.f;
; #pragma unroll
;                 for (int bj = 0; bj < 2; ++bj)
; #pragma unroll
;                     for (int n = 0; n < 2; ++n) { const size_t o = (size_t)r * cfg::DM + col0 + bj * HALF + n * 16; const f32x4 xn = xo[m * 4 + bj * 2 + n] + acc[ai][bj][m][n];
;                         if (W_F32) *(f32x4*)(xnew + o) = xn;
;                         if (W_BF16) { u32x2 w; w.x = cvt_pk_bf16(xn[0], xn[1]); w.y = cvt_pk_bf16(xn[2], xn[3]); *(u32x2*)(xb + o) = w; }
;                         s += (xn[0] * xn[0] + xn[1] * xn[1]) + (xn[2] * xn[2] + xn[3] * xn[3]); }
;                 s += __shfl_xor(s, 16); s += __shfl_xor(s, 32);
;                 if (fq == 0) red[wc * 256 + (r - u.pm * BM)] = s; }
.LBB0_1683:
	s_lshl_b32 s12, s40, 8
	v_lshl_or_b32 v140, s39, 8, v177
	v_add_u32_e32 v142, s12, v1
	v_ashrrev_i32_e32 v141, 31, v140
	v_lshlrev_b64 v[184:185], 1, v[140:141]
	v_ashrrev_i32_e32 v143, 31, v142
	v_lshl_add_u64 v[144:145], s[8:9], 0, v[184:185]
	v_lshlrev_b64 v[186:187], 13, v[142:143]
	v_lshl_add_u64 v[146:147], v[144:145], 0, v[186:187]
	global_load_dwordx4 v[188:191], v[146:147], off nt
	global_load_dwordx4 v[192:195], v[146:147], off offset:256 nt
	v_or_b32_e32 v146, 16, v142
	v_or_b32_e32 v148, 32, v142
	v_or_b32_e32 v150, 48, v142
	v_ashrrev_i32_e32 v147, 31, v146
	v_ashrrev_i32_e32 v149, 31, v148
	v_ashrrev_i32_e32 v151, 31, v150
	v_lshlrev_b64 v[166:167], 13, v[146:147]
	v_lshlrev_b64 v[156:157], 13, v[148:149]
	v_lshlrev_b64 v[146:147], 13, v[150:151]
	v_lshl_add_u64 v[148:149], v[144:145], 0, v[166:167]
	v_lshl_add_u64 v[150:151], v[144:145], 0, v[156:157]
	v_lshl_add_u64 v[182:183], v[144:145], 0, v[146:147]
	global_load_dwordx4 v[172:175], v[148:149], off nt
	global_load_dwordx4 v[168:171], v[148:149], off offset:256 nt
	global_load_dwordx4 v[162:165], v[150:151], off nt
	global_load_dwordx4 v[158:161], v[150:151], off offset:256 nt
	global_load_dwordx4 v[152:155], v[182:183], off nt
	s_nop 0
	global_load_dwordx4 v[148:151], v[182:183], off offset:256 nt
	v_and_b32_e32 v182, 64, v229
	v_xor_b32_e32 v181, 16, v229
	v_add_u32_e32 v182, 64, v182
	v_xor_b32_e32 v183, 32, v229
	v_cmp_lt_i32_e32 vcc, v181, v182
	v_lshl_add_u64 v[186:187], s[8:9], 0, v[186:187]
	v_lshl_add_u64 v[184:185], v[186:187], 0, v[184:185]
	v_cndmask_b32_e32 v181, v229, v181, vcc
	v_cmp_lt_i32_e32 vcc, v183, v182
	v_lshlrev_b32_e32 v182, 2, v181
	s_waitcnt vmcnt(0)
	v_swap_b32 v172, v174
	v_swap_b32 v173, v175
	v_swap_b32 v168, v170
	v_swap_b32 v169, v171
	v_swap_b32 v162, v164
	v_swap_b32 v163, v165
	v_swap_b32 v158, v160
	v_swap_b32 v159, v161
	v_swap_b32 v152, v154
	v_swap_b32 v153, v155
	v_swap_b32 v148, v150
	v_swap_b32 v149, v151
	v_lshlrev_b32_e32 v186, 16, v188
	v_and_b32_e32 v187, 0xffff0000, v188
	v_lshlrev_b32_e32 v188, 16, v189
	v_and_b32_e32 v189, 0xffff0000, v189
	v_lshlrev_b32_e32 v196, 16, v190
	v_and_b32_e32 v197, 0xffff0000, v190
	v_lshlrev_b32_e32 v190, 16, v191
	v_and_b32_e32 v191, 0xffff0000, v191
	v_cndmask_b32_e32 v183, v229, v183, vcc
	v_lshlrev_b32_e32 v198, 16, v192
	v_and_b32_e32 v199, 0xffff0000, v192
	v_lshlrev_b32_e32 v192, 16, v193
	v_and_b32_e32 v193, 0xffff0000, v193
	v_pk_add_f32 v[130:131], v[130:131], v[188:189]
	v_pk_add_f32 v[128:129], v[128:129], v[186:187]
	v_pk_add_f32 v[126:127], v[126:127], v[190:191]
	v_pk_add_f32 v[124:125], v[124:125], v[196:197]
	v_lshlrev_b32_e32 v181, 2, v183
	v_pk_add_f32 v[122:123], v[122:123], v[192:193]
	v_pk_add_f32 v[120:121], v[120:121], v[198:199]
	v_cvt_pk_bf16_f32 v186, v128, v129
	v_cvt_pk_bf16_f32 v187, v130, v131
	v_mul_f32_e32 v129, v129, v129
	v_mul_f32_e32 v131, v131, v131
	v_cvt_pk_bf16_f32 v188, v124, v125
	v_mul_f32_e32 v125, v125, v125
	v_mul_f32_e32 v183, v127, v127
	v_mul_f32_e32 v189, v121, v121
	v_mul_f32_e32 v190, v123, v123
	v_fmac_f32_e32 v129, v128, v128
	v_fmac_f32_e32 v131, v130, v130
	v_fmac_f32_e32 v125, v124, v124
	v_fmac_f32_e32 v183, v126, v126
	v_fmac_f32_e32 v189, v120, v120
	v_fmac_f32_e32 v190, v122, v122
	v_add_f32_e32 v124, v129, v131
	v_add_f32_e32 v125, v125, v183
	v_lshlrev_b32_e32 v200, 16, v194
	v_and_b32_e32 v201, 0xffff0000, v194
	v_lshlrev_b32_e32 v194, 16, v195
	v_and_b32_e32 v195, 0xffff0000, v195
	v_add_f32_e32 v124, v124, v125
	v_add_f32_e32 v125, v189, v190
	v_add_f32_e32 v128, v124, v125
	v_pk_add_f32 v[118:119], v[118:119], v[194:195]
	v_pk_add_f32 v[124:125], v[116:117], v[200:201]
	v_mul_f32_e32 v117, v119, v119
	v_mul_f32_e32 v116, v125, v125
	v_fmac_f32_e32 v116, v124, v124
	v_fmac_f32_e32 v117, v118, v118
	v_add_f32_e32 v116, v116, v117
	v_add_f32_e32 v116, v128, v116
	ds_bpermute_b32 v117, v182, v116
	v_cvt_pk_bf16_f32 v120, v120, v121
	v_cvt_pk_bf16_f32 v121, v122, v123
	v_cvt_pk_bf16_f32 v189, v126, v127
	v_mov_b32_e32 v206, v120
	v_mov_b32_e32 v207, v121
	s_waitcnt lgkmcnt(0)
	v_add_f32_e32 v116, v116, v117
	ds_bpermute_b32 v117, v181, v116
	v_cvt_pk_bf16_f32 v120, v124, v125
	v_cvt_pk_bf16_f32 v121, v118, v119
	v_mov_b32_e32 v202, v186
	v_mov_b32_e32 v203, v187
	v_mov_b32_e32 v204, v188
	v_mov_b32_e32 v205, v189
	global_store_dwordx4 v[184:185], v[202:205], off
	v_mov_b32_e32 v208, v120
	v_mov_b32_e32 v209, v121
	global_store_dwordx4 v[184:185], v[206:209], off offset:256
	s_and_saveexec_b64 s[22:23], s[0:1]
	s_cbranch_execz .LBB0_1685
	s_waitcnt lgkmcnt(0)
	v_add_f32_e32 v116, v116, v117
	ds_write_b32 v178, v116

; __device__ __forceinline__ unsigned cvt_pk_bf16(float lo, float hi) { f32x2_t v = {lo, hi}; bf16x2_t b = __builtin_convertvector(v, bf16x2_t); return __builtin_bit_cast(unsigned, b); }
; __device__ __forceinline__ float bf_lo(unsigned w) { return __uint_as_float(w << 16); }
; __device__ __forceinline__ float bf_hi(unsigned w) { return __uint_as_float(w & 0xffff0000u); }
;     __device__ __forceinline__ void operator()(const f32x4 (&acc)[2][2][4][2], const Unit& u, int wr, int wc, int fr, int fq) const {
;     ...
;             for (int i = 0; i < 16; ++i) { const int m = i >> 2, bj = (i >> 1) & 1, n = i & 1; const size_t o = (size_t)(row0 + ai * HALF + m * 16) * cfg::DM + col0 + bj * HALF + n * 16;
;                 if (OLD_BF16) { const u32x2 ww = *(const u32x2*)(xoldb + o); xo[i] = (f32x4){bf_lo(ww.x), bf_hi(ww.x), bf_lo(ww.y), bf_hi(ww.y)}; } else xo[i] = *(const f32x4*)(xold + o); }
;             asm volatile("" ::: "memory");
; #pragma unroll
;             for (int m = 0; m < 4; ++m) { const int r = row0 + ai * HALF + m * 16; float s = 0.f;
; #pragma unroll
;                 for (int bj = 0; bj < 2; ++bj)
; #pragma unroll
;                     for (int n = 0; n < 2; ++n) { const size_t o = (size_t)r * cfg::DM + col0 + bj * HALF + n * 16; const f32x4 xn = xo[m * 4 + bj * 2 + n] + acc[ai][bj][m][n];
;                         if (W_F32) *(f32x4*)(xnew + o) = xn;
;                         if (W_BF16) { u32x2 w; w.x = cvt_pk_bf16(xn[0], xn[1]); w.y = cvt_pk_bf16(xn[2], xn[3]); *(u32x2*)(xb + o) = w; }
;                         s += (xn[0] * xn[0] + xn[1] * xn[1]) + (xn[2] * xn[2] + xn[3] * xn[3]); }
;                 s += __shfl_xor(s, 16); s += __shfl_xor(s, 32);
;                 if (fq == 0) red[wc * 256 + (r - u.pm * BM)] = s; }
.LBB0_1691:
	s_or_b64 exec, exec, s[22:23]
	v_lshlrev_b64 v[84:85], 13, v[142:143]
	s_mov_b64 s[22:23], 0x100000
	v_lshl_add_u64 v[94:95], v[84:85], 0, s[22:23]
	s_waitcnt lgkmcnt(0)
	v_lshl_add_u64 v[68:69], v[144:145], 0, v[94:95]
	global_load_dwordx4 v[96:99], v[68:69], off nt
	global_load_dwordx4 v[100:103], v[68:69], off offset:256 nt
	v_add_u32_e32 v68, 0x90, v142
	v_add_u32_e32 v70, 0xa0, v142
	v_add_u32_e32 v72, 0xb0, v142
	v_ashrrev_i32_e32 v69, 31, v68
	v_ashrrev_i32_e32 v71, 31, v70
	v_ashrrev_i32_e32 v73, 31, v72
	v_lshlrev_b64 v[68:69], 13, v[68:69]
	v_lshlrev_b64 v[70:71], 13, v[70:71]
	v_lshlrev_b64 v[72:73], 13, v[72:73]
	v_lshl_add_u64 v[68:69], v[144:145], 0, v[68:69]
	v_lshl_add_u64 v[70:71], v[144:145], 0, v[70:71]
	v_lshl_add_u64 v[104:105], v[144:145], 0, v[72:73]
	global_load_dwordx4 v[90:93], v[68:69], off nt
	global_load_dwordx4 v[86:89], v[68:69], off offset:256 nt
	global_load_dwordx4 v[80:83], v[70:71], off nt
	global_load_dwordx4 v[76:79], v[70:71], off offset:256 nt
	global_load_dwordx4 v[72:75], v[104:105], off nt
	s_nop 0
	global_load_dwordx4 v[68:71], v[104:105], off offset:256 nt
	v_lshl_add_u64 v[94:95], s[8:9], 0, v[94:95]
	v_lshl_add_u64 v[94:95], v[140:141], 1, v[94:95]
	s_waitcnt vmcnt(7)
	v_lshlrev_b32_e32 v104, 16, v96
	v_and_b32_e32 v105, 0xffff0000, v96
	v_lshlrev_b32_e32 v96, 16, v97
	v_and_b32_e32 v97, 0xffff0000, v97
	v_lshlrev_b32_e32 v106, 16, v98
	v_and_b32_e32 v107, 0xffff0000, v98
	v_lshlrev_b32_e32 v98, 16, v99
	v_and_b32_e32 v99, 0xffff0000, v99
	s_waitcnt vmcnt(6)
	v_lshlrev_b32_e32 v108, 16, v100
	v_and_b32_e32 v109, 0xffff0000, v100
	v_lshlrev_b32_e32 v100, 16, v101
	v_and_b32_e32 v101, 0xffff0000, v101
	v_lshlrev_b32_e32 v110, 16, v102
	v_and_b32_e32 v111, 0xffff0000, v102
	v_pk_add_f32 v[66:67], v[66:67], v[96:97]
	v_pk_add_f32 v[64:65], v[64:65], v[104:105]
	v_pk_add_f32 v[62:63], v[62:63], v[98:99]
	v_pk_add_f32 v[60:61], v[60:61], v[106:107]
	v_lshlrev_b32_e32 v102, 16, v103
	v_and_b32_e32 v103, 0xffff0000, v103
	v_pk_add_f32 v[58:59], v[58:59], v[100:101]
	v_pk_add_f32 v[56:57], v[56:57], v[108:109]
	v_pk_add_f32 v[96:97], v[52:53], v[110:111]
	v_cvt_pk_bf16_f32 v52, v64, v65
	v_cvt_pk_bf16_f32 v53, v66, v67
	v_mul_f32_e32 v65, v65, v65
	v_mul_f32_e32 v67, v67, v67
	v_cvt_pk_bf16_f32 v98, v60, v61
	v_mul_f32_e32 v61, v61, v61
	v_mul_f32_e32 v99, v63, v63
	v_pk_add_f32 v[54:55], v[54:55], v[102:103]
	v_mul_f32_e32 v100, v57, v57
	v_mul_f32_e32 v101, v59, v59
	v_fmac_f32_e32 v65, v64, v64
	v_fmac_f32_e32 v67, v66, v66
	v_fmac_f32_e32 v61, v60, v60
	v_fmac_f32_e32 v99, v62, v62
	v_mul_f32_e32 v102, v97, v97
	v_mul_f32_e32 v103, v55, v55
	v_mov_b32_e32 v202, v52
	v_mov_b32_e32 v203, v53
	v_fmac_f32_e32 v100, v56, v56
	v_fmac_f32_e32 v101, v58, v58
	v_add_f32_e32 v52, v65, v67
	v_add_f32_e32 v53, v61, v99
	v_fmac_f32_e32 v102, v96, v96
	v_fmac_f32_e32 v103, v54, v54
	v_add_f32_e32 v60, v100, v101
	v_add_f32_e32 v52, v52, v53
	v_add_f32_e32 v52, v52, v60
	v_add_f32_e32 v53, v102, v103
	v_add_f32_e32 v52, v52, v53
	ds_bpermute_b32 v53, v182, v52
	v_cvt_pk_bf16_f32 v56, v56, v57
	v_cvt_pk_bf16_f32 v57, v58, v59
	v_cvt_pk_bf16_f32 v99, v62, v63
	v_mov_b32_e32 v206, v56
	v_mov_b32_e32 v207, v57
	s_waitcnt lgkmcnt(0)
	v_add_f32_e32 v52, v52, v53
	ds_bpermute_b32 v53, v181, v52
	v_cvt_pk_bf16_f32 v56, v96, v97
	v_cvt_pk_bf16_f32 v57, v54, v55
	v_mov_b32_e32 v204, v98
	v_mov_b32_e32 v205, v99
	global_store_dwordx4 v[94:95], v[202:205], off
	v_mov_b32_e32 v208, v56
	v_mov_b32_e32 v209, v57
	global_store_dwordx4 v[94:95], v[206:209], off offset:256
	s_and_saveexec_b64 s[22:23], s[0:1]
	s_cbranch_execz .LBB0_1693
	s_waitcnt lgkmcnt(0)
	v_add_f32_e32 v52, v52, v53
	ds_write_b32 v178, v52 offset:512

; #define INP(k) launder_p(args.in[k])
; __device__ __forceinline__ void final_rows(const bf16_t* x, const float* ss, const float* g, float* out, int r0, int step, int lane) {
;     f32x4 gv[16]; u32x4 va[8], vb[8];
; #pragma unroll
;     for (int j = 0; j < 8; ++j) { gv[2 * j] = ((const f32x4*)g)[2 * (64 * j + lane)]; gv[2 * j + 1] = ((const f32x4*)g)[2 * (64 * j + lane) + 1]; }
;     float sa = 0.f, sb = 0.f;
;     if (r0 < MT) { sa = ss[r0];
; #pragma unroll
;         for (int j = 0; j < 8; ++j) va[j] = ((const u32x4*)(x + (size_t)r0 * DM))[64 * j + lane]; }
; __global__ void __launch_bounds__(NWAVES * 64, 2) mega_fwd(Args args) {
;     ...
;     if (IN(11)) { PHASE_CTX(); const float* fg = INP(17); float* outp = args.out; final_rows((const bf16_t*)(ws + WS_XB), (const float*)(ws + WS_CTL + CTL_SS2), fg, outp, gw, NGW, lane); }
.LBB0_1757:
	v_readlane_b32 s0, v252, 2
	v_readlane_b32 s1, v252, 3
	s_mov_b64 s[4:5], s[0:1]
	s_cmp_lt_i32 s4, 12
	v_readlane_b32 s2, v252, 4
	v_readlane_b32 s3, v252, 5
	s_cselect_b64 s[0:1], -1, 0
	s_cmp_gt_i32 s5, 11
	s_cselect_b64 s[2:3], -1, 0
	s_and_b64 s[0:1], s[0:1], s[2:3]
	s_and_b64 vcc, exec, s[0:1]
	v_readlane_b32 s18, v252, 51
	v_readlane_b32 s19, v252, 52
	s_cbranch_vccz .LBB0_1769
	v_readlane_b32 s8, v252, 6
	v_readlane_b32 s10, v252, 8
	v_readlane_b32 s11, v252, 9
	v_readlane_b32 s14, v252, 12
	v_readlane_b32 s15, v252, 13
	s_waitcnt vmcnt(0)
	v_and_b32_e32 v1, 63, v0
	v_lshlrev_b32_e32 v132, 1, v1
	v_lshlrev_b32_e32 v18, 5, v1
	s_waitcnt lgkmcnt(0)
	global_load_dwordx4 v[2:5], v18, s[10:11] offset:16
	global_load_dwordx4 v[6:9], v18, s[10:11]
	global_load_dwordx4 v[10:13], v18, s[10:11] offset:2064
	global_load_dwordx4 v[14:17], v18, s[10:11] offset:2048
	v_or_b32_e32 v18, 0x100, v132
	v_or_b32_e32 v26, 0x180, v132
	v_or_b32_e32 v34, 0x200, v132
	v_or_b32_e32 v42, 0x280, v132
	v_or_b32_e32 v50, 0x300, v132
	v_or_b32_e32 v58, 0x380, v132
	v_lshlrev_b32_e32 v133, 4, v18
	v_lshlrev_b32_e32 v134, 4, v26
	v_lshlrev_b32_e32 v135, 4, v34
	v_lshlrev_b32_e32 v136, 4, v42
	v_lshlrev_b32_e32 v137, 4, v50
	v_lshlrev_b32_e32 v138, 4, v58
	global_load_dwordx4 v[18:21], v133, s[10:11] offset:16
	global_load_dwordx4 v[22:25], v133, s[10:11]
	global_load_dwordx4 v[26:29], v134, s[10:11] offset:16
	global_load_dwordx4 v[30:33], v134, s[10:11]
	global_load_dwordx4 v[34:37], v135, s[10:11] offset:16
	global_load_dwordx4 v[38:41], v135, s[10:11]
	global_load_dwordx4 v[42:45], v136, s[10:11] offset:16
	global_load_dwordx4 v[46:49], v136, s[10:11]
	global_load_dwordx4 v[50:53], v137, s[10:11] offset:16
	global_load_dwordx4 v[54:57], v137, s[10:11]
	global_load_dwordx4 v[58:61], v138, s[10:11] offset:16
	global_load_dwordx4 v[62:65], v138, s[10:11]
	v_readfirstlane_b32 s0, v0
	s_ashr_i32 s0, s0, 6
	s_lshl_b32 s1, s82, 3
	s_add_i32 s0, s0, s1
	s_add_u32 s2, s14, 0x27100000
	s_addc_u32 s3, s15, 0
	v_readlane_b32 s9, v252, 7
	s_add_u32 s8, s14, 0x90000
	s_addc_u32 s9, s15, 0
	v_mov_b32_e32 v139, 0
	s_cmpk_lt_i32 s0, 0x2000
	v_readlane_b32 s12, v252, 10
	v_readlane_b32 s13, v252, 11
	s_cselect_b64 s[4:5], -1, 0
	s_cmpk_gt_i32 s0, 0x1fff
	v_lshlrev_b32_e32 v0, 4, v1
	v_mov_b32_e32 v66, 0
	v_mov_b32_e32 v67, v139
	v_mov_b32_e32 v68, v139
	v_mov_b32_e32 v69, v139
	v_mov_b32_e32 v70, 0
	v_mov_b32_e32 v71, v139
	v_mov_b32_e32 v72, v139
	v_mov_b32_e32 v73, v139
	v_mov_b32_e32 v74, 0
	v_mov_b32_e32 v75, v139
	v_mov_b32_e32 v76, v139
	v_mov_b32_e32 v77, v139
	v_mov_b32_e32 v78, 0
	v_mov_b32_e32 v79, v139
	v_mov_b32_e32 v80, v139
	v_mov_b32_e32 v81, v139
	v_mov_b32_e32 v82, 0
	v_mov_b32_e32 v83, v139
	v_mov_b32_e32 v84, v139
	v_mov_b32_e32 v85, v139
	v_mov_b32_e32 v86, 0
	v_mov_b32_e32 v87, v139
	v_mov_b32_e32 v88, v139
	v_mov_b32_e32 v89, v139
	v_mov_b32_e32 v90, 0
	v_mov_b32_e32 v91, v139
	v_mov_b32_e32 v92, v139
	v_mov_b32_e32 v93, v139
	v_mov_b32_e32 v94, 0
	v_mov_b32_e32 v95, v139
	v_mov_b32_e32 v96, v139
	v_mov_b32_e32 v97, v139
	s_cbranch_scc1 .LBB0_1760
	s_ashr_i32 s1, s0, 31
	s_lshl_b64 s[6:7], s[0:1], 2
	s_add_u32 s6, s8, s6
	s_addc_u32 s7, s9, s7
	s_lshl_b64 s[10:11], s[0:1], 13
	s_add_u32 s10, s2, s10
	v_mov_b32_e32 v1, 0
	s_addc_u32 s11, s3, s11
	v_lshl_add_u64 v[82:83], s[10:11], 0, v[0:1]
	s_movk_i32 s1, 0x1000
	v_add_co_u32_e32 v98, vcc, s1, v82
	global_load_dword v139, v1, s[6:7]
	global_load_dwordx4 v[66:69], v0, s[10:11] nt
	global_load_dwordx4 v[70:73], v0, s[10:11] offset:1024 nt
	global_load_dwordx4 v[74:77], v0, s[10:11] offset:2048 nt
	global_load_dwordx4 v[78:81], v0, s[10:11] offset:3072 nt
	v_addc_co_u32_e32 v99, vcc, 0, v83, vcc
	global_load_dwordx4 v[82:85], v[98:99], off nt
	global_load_dwordx4 v[86:89], v[98:99], off offset:1024 nt
	global_load_dwordx4 v[90:93], v[98:99], off offset:2048 nt
	global_load_dwordx4 v[94:97], v[98:99], off offset:3072 nt

.LBB0_1762:
	v_fmamk_f32 v0, v141, 0x39800000, v140
	v_rsq_f32_e32 v0, v0
	s_ashr_i32 s3, s2, 31
	s_add_i32 s4, s2, s18
	s_lshl_b64 s[0:1], s[2:3], 14
	s_mov_b64 s[16:17], s[12:13]
	v_lshlrev_b32_e32 v144, 16, v110
	v_and_b32_e32 v145, 0xffff0000, v110
	v_lshlrev_b32_e32 v146, 16, v111
	v_and_b32_e32 v147, 0xffff0000, v111
	s_add_u32 s0, s16, s0
	v_pk_mul_f32 v[144:145], v[0:1], v[144:145] op_sel_hi:[0,1]
	v_pk_mul_f32 v[146:147], v[0:1], v[146:147] op_sel_hi:[0,1]
	s_addc_u32 s1, s17, s1
	v_pk_mul_f32 v[146:147], v[8:9], v[146:147]
	v_pk_mul_f32 v[144:145], v[6:7], v[144:145]
	global_store_dwordx4 v142, v[144:147], s[0:1] nt
	v_and_b32_e32 v143, 0xffff0000, v102
	s_cmpk_gt_i32 s4, 0x1fff
	v_lshlrev_b32_e32 v144, 16, v112
	v_and_b32_e32 v145, 0xffff0000, v112
	v_lshlrev_b32_e32 v146, 16, v113
	v_and_b32_e32 v147, 0xffff0000, v113
	v_pk_mul_f32 v[144:145], v[0:1], v[144:145] op_sel_hi:[0,1]
	v_pk_mul_f32 v[146:147], v[0:1], v[146:147] op_sel_hi:[0,1]
	v_pk_mul_f32 v[146:147], v[4:5], v[146:147]
	v_pk_mul_f32 v[144:145], v[2:3], v[144:145]
	global_store_dwordx4 v142, v[144:147], s[0:1] offset:16 nt
	s_nop 1
	v_lshlrev_b32_e32 v144, 16, v106
	v_and_b32_e32 v145, 0xffff0000, v106
	v_lshlrev_b32_e32 v146, 16, v107
	v_and_b32_e32 v147, 0xffff0000, v107
	v_pk_mul_f32 v[144:145], v[0:1], v[144:145] op_sel_hi:[0,1]
	v_pk_mul_f32 v[146:147], v[0:1], v[146:147] op_sel_hi:[0,1]
	v_pk_mul_f32 v[146:147], v[16:17], v[146:147]
	v_pk_mul_f32 v[144:145], v[14:15], v[144:145]
	global_store_dwordx4 v142, v[144:147], s[0:1] offset:2048 nt
	s_nop 1
	v_lshlrev_b32_e32 v144, 16, v108
	v_and_b32_e32 v145, 0xffff0000, v108
	v_lshlrev_b32_e32 v146, 16, v109
	v_and_b32_e32 v147, 0xffff0000, v109
	v_pk_mul_f32 v[144:145], v[0:1], v[144:145] op_sel_hi:[0,1]
	v_pk_mul_f32 v[146:147], v[0:1], v[146:147] op_sel_hi:[0,1]
	v_pk_mul_f32 v[146:147], v[12:13], v[146:147]
	v_pk_mul_f32 v[144:145], v[10:11], v[144:145]
	global_store_dwordx4 v142, v[144:147], s[0:1] offset:2064 nt
	v_lshlrev_b32_e32 v142, 16, v102
	v_pk_mul_f32 v[142:143], v[0:1], v[142:143] op_sel_hi:[0,1]
	v_lshlrev_b32_e32 v144, 16, v103
	v_and_b32_e32 v145, 0xffff0000, v103
	v_pk_mul_f32 v[144:145], v[0:1], v[144:145] op_sel_hi:[0,1]
	v_pk_mul_f32 v[144:145], v[24:25], v[144:145]
	v_pk_mul_f32 v[142:143], v[22:23], v[142:143]
	global_store_dwordx4 v133, v[142:145], s[0:1] nt
	s_nop 1
	v_lshlrev_b32_e32 v142, 16, v104
	v_and_b32_e32 v143, 0xffff0000, v104
	v_lshlrev_b32_e32 v144, 16, v105
	v_and_b32_e32 v145, 0xffff0000, v105
	v_pk_mul_f32 v[142:143], v[0:1], v[142:143] op_sel_hi:[0,1]
	v_pk_mul_f32 v[144:145], v[0:1], v[144:145] op_sel_hi:[0,1]
	v_pk_mul_f32 v[144:145], v[20:21], v[144:145]
	v_pk_mul_f32 v[142:143], v[18:19], v[142:143]
	global_store_dwordx4 v133, v[142:145], s[0:1] offset:16 nt
	s_nop 1
	v_lshlrev_b32_e32 v142, 16, v98
	v_and_b32_e32 v143, 0xffff0000, v98
	v_lshlrev_b32_e32 v144, 16, v99
	v_and_b32_e32 v145, 0xffff0000, v99
	v_pk_mul_f32 v[142:143], v[0:1], v[142:143] op_sel_hi:[0,1]
	v_pk_mul_f32 v[144:145], v[0:1], v[144:145] op_sel_hi:[0,1]
	v_pk_mul_f32 v[144:145], v[32:33], v[144:145]
	v_pk_mul_f32 v[142:143], v[30:31], v[142:143]
	global_store_dwordx4 v134, v[142:145], s[0:1] nt
	s_nop 1
	v_lshlrev_b32_e32 v142, 16, v100
	v_and_b32_e32 v143, 0xffff0000, v100
	v_lshlrev_b32_e32 v144, 16, v101
	v_and_b32_e32 v145, 0xffff0000, v101
	v_pk_mul_f32 v[142:143], v[0:1], v[142:143] op_sel_hi:[0,1]
	v_pk_mul_f32 v[144:145], v[0:1], v[144:145] op_sel_hi:[0,1]
	v_pk_mul_f32 v[144:145], v[28:29], v[144:145]
	v_pk_mul_f32 v[142:143], v[26:27], v[142:143]
	global_store_dwordx4 v134, v[142:145], s[0:1] offset:16 nt
	s_nop 1
	v_lshlrev_b32_e32 v142, 16, v126
	v_and_b32_e32 v143, 0xffff0000, v126
	v_lshlrev_b32_e32 v144, 16, v127
	v_and_b32_e32 v145, 0xffff0000, v127
	v_pk_mul_f32 v[142:143], v[0:1], v[142:143] op_sel_hi:[0,1]
	v_pk_mul_f32 v[144:145], v[0:1], v[144:145] op_sel_hi:[0,1]
	v_pk_mul_f32 v[144:145], v[40:41], v[144:145]
	v_pk_mul_f32 v[142:143], v[38:39], v[142:143]
	global_store_dwordx4 v135, v[142:145], s[0:1] nt
	s_nop 1
	v_lshlrev_b32_e32 v142, 16, v128
	v_and_b32_e32 v143, 0xffff0000, v128
	v_lshlrev_b32_e32 v144, 16, v129
	v_and_b32_e32 v145, 0xffff0000, v129
	v_pk_mul_f32 v[142:143], v[0:1], v[142:143] op_sel_hi:[0,1]
	v_pk_mul_f32 v[144:145], v[0:1], v[144:145] op_sel_hi:[0,1]
	v_pk_mul_f32 v[144:145], v[36:37], v[144:145]
	v_pk_mul_f32 v[142:143], v[34:35], v[142:143]
	global_store_dwordx4 v135, v[142:145], s[0:1] offset:16 nt
	s_nop 1
	v_lshlrev_b32_e32 v142, 16, v122
	v_and_b32_e32 v143, 0xffff0000, v122
	v_lshlrev_b32_e32 v144, 16, v123
	v_and_b32_e32 v145, 0xffff0000, v123
	v_pk_mul_f32 v[142:143], v[0:1], v[142:143] op_sel_hi:[0,1]
	v_pk_mul_f32 v[144:145], v[0:1], v[144:145] op_sel_hi:[0,1]
	v_pk_mul_f32 v[144:145], v[48:49], v[144:145]
	v_pk_mul_f32 v[142:143], v[46:47], v[142:143]
	global_store_dwordx4 v136, v[142:145], s[0:1] nt
	s_nop 1
	v_lshlrev_b32_e32 v142, 16, v124
	v_and_b32_e32 v143, 0xffff0000, v124
	v_lshlrev_b32_e32 v144, 16, v125
	v_and_b32_e32 v145, 0xffff0000, v125
	v_pk_mul_f32 v[142:143], v[0:1], v[142:143] op_sel_hi:[0,1]
	v_pk_mul_f32 v[144:145], v[0:1], v[144:145] op_sel_hi:[0,1]
	v_pk_mul_f32 v[144:145], v[44:45], v[144:145]
	v_pk_mul_f32 v[142:143], v[42:43], v[142:143]
	global_store_dwordx4 v136, v[142:145], s[0:1] offset:16 nt
	s_nop 1
	v_lshlrev_b32_e32 v142, 16, v118
	v_and_b32_e32 v143, 0xffff0000, v118
	v_lshlrev_b32_e32 v144, 16, v119
	v_and_b32_e32 v145, 0xffff0000, v119
	v_pk_mul_f32 v[142:143], v[0:1], v[142:143] op_sel_hi:[0,1]
	v_pk_mul_f32 v[144:145], v[0:1], v[144:145] op_sel_hi:[0,1]
	v_pk_mul_f32 v[144:145], v[56:57], v[144:145]
; __device__ __forceinline__ void final_rows(const bf16_t* x, const float* ss, const float* g, float* out, int r0, int step, int lane) {
;     ...
;     for (int r = r0; r < MT; r += 2 * step) {
;         const int r1 = r + step, r2 = r + 2 * step;
;         if (r1 < MT) { sb = ss[r1];
; #pragma unroll
;             for (int j = 0; j < 8; ++j) vb[j] = ((const u32x4*)(x + (size_t)r1 * DM))[64 * j + lane]; }
	v_pk_mul_f32 v[142:143], v[54:55], v[142:143]
	global_store_dwordx4 v137, v[142:145], s[0:1] nt
	s_nop 1
	v_lshlrev_b32_e32 v142, 16, v120
	v_and_b32_e32 v143, 0xffff0000, v120
	v_lshlrev_b32_e32 v144, 16, v121
	v_and_b32_e32 v145, 0xffff0000, v121
	v_pk_mul_f32 v[142:143], v[0:1], v[142:143] op_sel_hi:[0,1]
	v_pk_mul_f32 v[144:145], v[0:1], v[144:145] op_sel_hi:[0,1]
	v_pk_mul_f32 v[144:145], v[52:53], v[144:145]
	v_pk_mul_f32 v[142:143], v[50:51], v[142:143]
	global_store_dwordx4 v137, v[142:145], s[0:1] offset:16 nt
	s_nop 1
	v_lshlrev_b32_e32 v142, 16, v114
	v_and_b32_e32 v143, 0xffff0000, v114
	v_lshlrev_b32_e32 v144, 16, v115
	v_and_b32_e32 v145, 0xffff0000, v115
	v_pk_mul_f32 v[142:143], v[0:1], v[142:143] op_sel_hi:[0,1]
	v_pk_mul_f32 v[144:145], v[0:1], v[144:145] op_sel_hi:[0,1]
	v_pk_mul_f32 v[144:145], v[64:65], v[144:145]
	v_pk_mul_f32 v[142:143], v[62:63], v[142:143]
	global_store_dwordx4 v138, v[142:145], s[0:1] nt
	s_nop 1
	v_lshlrev_b32_e32 v142, 16, v116
	v_and_b32_e32 v143, 0xffff0000, v116
	v_lshlrev_b32_e32 v144, 16, v117
	v_and_b32_e32 v145, 0xffff0000, v117
	v_pk_mul_f32 v[142:143], v[0:1], v[142:143] op_sel_hi:[0,1]
	v_pk_mul_f32 v[144:145], v[0:1], v[144:145] op_sel_hi:[0,1]
	v_pk_mul_f32 v[144:145], v[60:61], v[144:145]
	v_pk_mul_f32 v[142:143], v[58:59], v[142:143]
	global_store_dwordx4 v138, v[142:145], s[0:1] offset:16 nt
	s_cselect_b64 s[0:1], -1, 0
	s_and_b64 vcc, exec, s[0:1]
	s_mov_b32 s0, s4
	s_cbranch_vccnz .LBB0_1769
.LBB0_1763:
	s_add_i32 s2, s0, s18
	s_cmpk_lt_i32 s2, 0x2000
	s_cselect_b64 s[4:5], -1, 0
	s_cmpk_gt_i32 s2, 0x1fff
	s_cbranch_scc1 .LBB0_1765
	s_ashr_i32 s3, s2, 31
	s_lshl_b64 s[6:7], s[2:3], 2
	s_add_u32 s6, s8, s6
	s_addc_u32 s7, s9, s7
	global_load_dword v141, v1, s[6:7]
	s_lshl_b64 s[6:7], s[2:3], 13
	v_lshl_add_u64 v[114:115], v[130:131], 0, s[6:7]
	global_load_dwordx4 v[110:113], v[114:115], off nt
	global_load_dwordx4 v[106:109], v[114:115], off offset:1024 nt
	global_load_dwordx4 v[102:105], v[114:115], off offset:2048 nt
	global_load_dwordx4 v[98:101], v[114:115], off offset:3072 nt
	v_add_co_u32_e32 v114, vcc, 0x1000, v114
	s_nop 1
	v_addc_co_u32_e32 v115, vcc, 0, v115, vcc
	global_load_dwordx4 v[126:129], v[114:115], off nt
	global_load_dwordx4 v[122:125], v[114:115], off offset:1024 nt
	global_load_dwordx4 v[118:121], v[114:115], off offset:2048 nt
	s_nop 0
	global_load_dwordx4 v[114:117], v[114:115], off offset:3072 nt
.LBB0_1765:
	s_waitcnt vmcnt(8)
	v_fmamk_f32 v0, v139, 0x39800000, v140
	v_rsq_f32_e32 v0, v0
	s_ashr_i32 s1, s0, 31
	s_lshl_b64 s[6:7], s[0:1], 14
	s_mov_b64 s[16:17], s[12:13]
	s_waitcnt vmcnt(7)
	v_lshlrev_b32_e32 v142, 16, v66
	v_and_b32_e32 v143, 0xffff0000, v66
	v_lshlrev_b32_e32 v144, 16, v67
	v_and_b32_e32 v145, 0xffff0000, v67
	s_add_u32 s6, s16, s6
	v_pk_mul_f32 v[142:143], v[0:1], v[142:143] op_sel_hi:[0,1]
	v_pk_mul_f32 v[144:145], v[0:1], v[144:145] op_sel_hi:[0,1]
	s_addc_u32 s7, s17, s7
	v_pk_mul_f32 v[146:147], v[8:9], v[144:145]
	v_pk_mul_f32 v[144:145], v[6:7], v[142:143]
	v_lshlrev_b32_e32 v142, 4, v132
	global_store_dwordx4 v142, v[144:147], s[6:7] nt
	s_andn2_b64 vcc, exec, s[4:5]
	v_readfirstlane_b32 s4, v0
	v_lshlrev_b32_e32 v144, 16, v68
	v_and_b32_e32 v145, 0xffff0000, v68
	v_lshlrev_b32_e32 v146, 16, v69
	v_and_b32_e32 v147, 0xffff0000, v69
	v_pk_mul_f32 v[144:145], v[0:1], v[144:145] op_sel_hi:[0,1]
	v_pk_mul_f32 v[146:147], v[0:1], v[146:147] op_sel_hi:[0,1]
	v_pk_mul_f32 v[146:147], v[4:5], v[146:147]
	v_pk_mul_f32 v[144:145], v[2:3], v[144:145]
	global_store_dwordx4 v142, v[144:147], s[6:7] offset:16 nt
	s_waitcnt vmcnt(8)
	s_nop 0
	v_lshlrev_b32_e32 v144, 16, v70
	v_and_b32_e32 v145, 0xffff0000, v70
	v_lshlrev_b32_e32 v146, 16, v71
	v_and_b32_e32 v147, 0xffff0000, v71
	v_pk_mul_f32 v[144:145], v[0:1], v[144:145] op_sel_hi:[0,1]
	v_pk_mul_f32 v[146:147], v[0:1], v[146:147] op_sel_hi:[0,1]
	v_pk_mul_f32 v[146:147], v[16:17], v[146:147]
	v_pk_mul_f32 v[144:145], v[14:15], v[144:145]
	global_store_dwordx4 v142, v[144:147], s[6:7] offset:2048 nt
	s_nop 1
	v_lshlrev_b32_e32 v144, 16, v72
	v_and_b32_e32 v145, 0xffff0000, v72
	v_lshlrev_b32_e32 v146, 16, v73
	v_and_b32_e32 v147, 0xffff0000, v73
	v_pk_mul_f32 v[144:145], v[0:1], v[144:145] op_sel_hi:[0,1]
	v_pk_mul_f32 v[146:147], v[0:1], v[146:147] op_sel_hi:[0,1]
	v_pk_mul_f32 v[146:147], v[12:13], v[146:147]
	v_pk_mul_f32 v[144:145], v[10:11], v[144:145]
	global_store_dwordx4 v142, v[144:147], s[6:7] offset:2064 nt
	s_waitcnt vmcnt(9)
	s_nop 0
	v_lshlrev_b32_e32 v144, 16, v74
	v_and_b32_e32 v145, 0xffff0000, v74
	v_lshlrev_b32_e32 v146, 16, v75
	v_and_b32_e32 v147, 0xffff0000, v75
	v_pk_mul_f32 v[144:145], v[0:1], v[144:145] op_sel_hi:[0,1]
	v_pk_mul_f32 v[146:147], v[0:1], v[146:147] op_sel_hi:[0,1]
	v_pk_mul_f32 v[146:147], v[24:25], v[146:147]
	v_pk_mul_f32 v[144:145], v[22:23], v[144:145]
	global_store_dwordx4 v133, v[144:147], s[6:7] nt
	s_nop 1
	v_lshlrev_b32_e32 v144, 16, v76
	v_and_b32_e32 v145, 0xffff0000, v76
	v_lshlrev_b32_e32 v146, 16, v77
	v_and_b32_e32 v147, 0xffff0000, v77
	v_pk_mul_f32 v[144:145], v[0:1], v[144:145] op_sel_hi:[0,1]
	v_pk_mul_f32 v[146:147], v[0:1], v[146:147] op_sel_hi:[0,1]
	v_pk_mul_f32 v[146:147], v[20:21], v[146:147]
	v_pk_mul_f32 v[144:145], v[18:19], v[144:145]
	global_store_dwordx4 v133, v[144:147], s[6:7] offset:16 nt
	s_waitcnt vmcnt(10)
; __device__ __forceinline__ void final_rows(const bf16_t* x, const float* ss, const float* g, float* out, int r0, int step, int lane) {
;     ...
;     for (int r = r0; r < MT; r += 2 * step) {
;         const int r1 = r + step, r2 = r + 2 * step;
;         if (r1 < MT) { sb = ss[r1];
; #pragma unroll
;             for (int j = 0; j < 8; ++j) vb[j] = ((const u32x4*)(x + (size_t)r1 * DM))[64 * j + lane]; }
;         asm volatile("" ::: "memory");
;         FIN_STORE(va, sa, r);
;         if (r1 >= MT) break;
;         if (r2 < MT) { sa = ss[r2];
; #pragma unroll
;             for (int j = 0; j < 8; ++j) va[j] = ((const u32x4*)(x + (size_t)r2 * DM))[64 * j + lane]; }
	s_nop 0
	v_lshlrev_b32_e32 v144, 16, v78
	v_and_b32_e32 v145, 0xffff0000, v78
	v_lshlrev_b32_e32 v146, 16, v79
	v_and_b32_e32 v147, 0xffff0000, v79
	v_pk_mul_f32 v[144:145], v[0:1], v[144:145] op_sel_hi:[0,1]
	v_pk_mul_f32 v[146:147], v[0:1], v[146:147] op_sel_hi:[0,1]
	v_pk_mul_f32 v[146:147], v[32:33], v[146:147]
	v_pk_mul_f32 v[144:145], v[30:31], v[144:145]
	global_store_dwordx4 v134, v[144:147], s[6:7] nt
	s_nop 1
	v_lshlrev_b32_e32 v144, 16, v80
	v_and_b32_e32 v145, 0xffff0000, v80
	v_lshlrev_b32_e32 v146, 16, v81
	v_and_b32_e32 v147, 0xffff0000, v81
	v_pk_mul_f32 v[144:145], v[0:1], v[144:145] op_sel_hi:[0,1]
	v_pk_mul_f32 v[146:147], v[0:1], v[146:147] op_sel_hi:[0,1]
	v_pk_mul_f32 v[146:147], v[28:29], v[146:147]
	v_pk_mul_f32 v[144:145], v[26:27], v[144:145]
	global_store_dwordx4 v134, v[144:147], s[6:7] offset:16 nt
	s_waitcnt vmcnt(11)
	s_nop 0
	v_lshlrev_b32_e32 v144, 16, v82
	v_and_b32_e32 v145, 0xffff0000, v82
	v_lshlrev_b32_e32 v146, 16, v83
	v_and_b32_e32 v147, 0xffff0000, v83
	v_pk_mul_f32 v[144:145], v[0:1], v[144:145] op_sel_hi:[0,1]
	v_pk_mul_f32 v[146:147], v[0:1], v[146:147] op_sel_hi:[0,1]
	v_pk_mul_f32 v[146:147], v[40:41], v[146:147]
	v_pk_mul_f32 v[144:145], v[38:39], v[144:145]
	global_store_dwordx4 v135, v[144:147], s[6:7] nt
	s_nop 1
	v_lshlrev_b32_e32 v144, 16, v84
	v_and_b32_e32 v145, 0xffff0000, v84
	v_lshlrev_b32_e32 v146, 16, v85
	v_and_b32_e32 v147, 0xffff0000, v85
	v_pk_mul_f32 v[144:145], v[0:1], v[144:145] op_sel_hi:[0,1]
	v_pk_mul_f32 v[146:147], v[0:1], v[146:147] op_sel_hi:[0,1]
	v_pk_mul_f32 v[146:147], v[36:37], v[146:147]
	v_pk_mul_f32 v[144:145], v[34:35], v[144:145]
	global_store_dwordx4 v135, v[144:147], s[6:7] offset:16 nt
	s_waitcnt vmcnt(12)
	s_nop 0
	v_lshlrev_b32_e32 v144, 16, v86
	v_and_b32_e32 v145, 0xffff0000, v86
	v_lshlrev_b32_e32 v146, 16, v87
	v_and_b32_e32 v147, 0xffff0000, v87
	v_pk_mul_f32 v[144:145], v[0:1], v[144:145] op_sel_hi:[0,1]
	v_pk_mul_f32 v[146:147], v[0:1], v[146:147] op_sel_hi:[0,1]
	v_pk_mul_f32 v[146:147], v[48:49], v[146:147]
	v_pk_mul_f32 v[144:145], v[46:47], v[144:145]
	global_store_dwordx4 v136, v[144:147], s[6:7] nt
	s_nop 1
	v_lshlrev_b32_e32 v144, 16, v88
	v_and_b32_e32 v145, 0xffff0000, v88
	v_lshlrev_b32_e32 v146, 16, v89
	v_and_b32_e32 v147, 0xffff0000, v89
	v_pk_mul_f32 v[144:145], v[0:1], v[144:145] op_sel_hi:[0,1]
	v_pk_mul_f32 v[146:147], v[0:1], v[146:147] op_sel_hi:[0,1]
	v_pk_mul_f32 v[146:147], v[44:45], v[146:147]
	v_pk_mul_f32 v[144:145], v[42:43], v[144:145]
	global_store_dwordx4 v136, v[144:147], s[6:7] offset:16 nt
	s_waitcnt vmcnt(13)
	s_nop 0
	v_lshlrev_b32_e32 v144, 16, v90
	v_and_b32_e32 v145, 0xffff0000, v90
	v_lshlrev_b32_e32 v146, 16, v91
	v_and_b32_e32 v147, 0xffff0000, v91
	v_pk_mul_f32 v[144:145], v[0:1], v[144:145] op_sel_hi:[0,1]
	v_pk_mul_f32 v[146:147], v[0:1], v[146:147] op_sel_hi:[0,1]
	v_pk_mul_f32 v[146:147], v[56:57], v[146:147]
	v_pk_mul_f32 v[144:145], v[54:55], v[144:145]
	global_store_dwordx4 v137, v[144:147], s[6:7] nt
	s_nop 1
	v_lshlrev_b32_e32 v144, 16, v92
	v_and_b32_e32 v145, 0xffff0000, v92
	v_lshlrev_b32_e32 v146, 16, v93
	v_and_b32_e32 v147, 0xffff0000, v93
	v_pk_mul_f32 v[144:145], v[0:1], v[144:145] op_sel_hi:[0,1]
	v_pk_mul_f32 v[146:147], v[0:1], v[146:147] op_sel_hi:[0,1]
	v_pk_mul_f32 v[146:147], v[52:53], v[146:147]
	v_pk_mul_f32 v[144:145], v[50:51], v[144:145]
	global_store_dwordx4 v137, v[144:147], s[6:7] offset:16 nt
	s_waitcnt vmcnt(14)
	s_nop 0
	v_lshlrev_b32_e32 v144, 16, v94
	v_and_b32_e32 v145, 0xffff0000, v94
	v_lshlrev_b32_e32 v146, 16, v95
	v_and_b32_e32 v147, 0xffff0000, v95
	v_pk_mul_f32 v[144:145], v[0:1], v[144:145] op_sel_hi:[0,1]
	v_pk_mul_f32 v[146:147], v[0:1], v[146:147] op_sel_hi:[0,1]
	v_pk_mul_f32 v[146:147], v[64:65], v[146:147]
	v_pk_mul_f32 v[144:145], v[62:63], v[144:145]
	global_store_dwordx4 v138, v[144:147], s[6:7] nt
	s_nop 1
	v_lshlrev_b32_e32 v144, 16, v96
	v_and_b32_e32 v145, 0xffff0000, v96
	v_lshlrev_b32_e32 v146, 16, v97
	v_and_b32_e32 v147, 0xffff0000, v97
	v_pk_mul_f32 v[144:145], v[0:1], v[144:145] op_sel_hi:[0,1]
	v_pk_mul_f32 v[146:147], v[0:1], v[146:147] op_sel_hi:[0,1]
	v_pk_mul_f32 v[146:147], v[60:61], v[146:147]
	v_pk_mul_f32 v[144:145], v[58:59], v[144:145]
	global_store_dwordx4 v138, v[144:147], s[6:7] offset:16 nt
	s_cbranch_vccnz .LBB0_1768
	s_add_i32 s0, s10, s0
	s_cmpk_gt_i32 s0, 0x1fff
	s_cbranch_scc1 .LBB0_1762
	s_ashr_i32 s1, s0, 31
	s_lshl_b64 s[4:5], s[0:1], 2
	s_add_u32 s4, s8, s4
	s_addc_u32 s5, s9, s5
	s_lshl_b64 s[0:1], s[0:1], 13
	v_lshl_add_u64 v[82:83], v[130:131], 0, s[0:1]
	v_add_co_u32_e32 v94, vcc, s11, v82
	global_load_dword v139, v1, s[4:5]
	s_nop 0
	v_addc_co_u32_e32 v95, vcc, 0, v83, vcc
	global_load_dwordx4 v[66:69], v[82:83], off nt
	global_load_dwordx4 v[70:73], v[82:83], off offset:1024 nt
	global_load_dwordx4 v[74:77], v[82:83], off offset:2048 nt
	global_load_dwordx4 v[78:81], v[82:83], off offset:3072 nt
	s_nop 0
	global_load_dwordx4 v[82:85], v[94:95], off nt
	global_load_dwordx4 v[86:89], v[94:95], off offset:1024 nt
	global_load_dwordx4 v[90:93], v[94:95], off offset:2048 nt
	s_nop 0
	global_load_dwordx4 v[94:97], v[94:95], off offset:3072 nt
	s_branch .LBB0_1762
